# baseline (speedup 1.0000x reference)
.LBB7_6:
	s_andn2_b64 vcc, exec, s[4:5]
	s_cbranch_vccnz .LBB7_70
	s_load_dwordx4 s[4:7], s[0:1], 0x0
	s_load_dwordx2 s[8:9], s[0:1], 0x10
	v_lshrrev_b32_e32 v80, 3, v0
	v_and_b32_e32 v81, 24, v80
	s_lshl_b32 s24, s2, 5
	v_and_b32_e32 v82, 63, v0
	v_or_b32_e32 v72, s24, v81
	v_lshlrev_b32_e32 v2, 5, v82
	v_mov_b32_e32 v3, 0
	v_ashrrev_i32_e32 v73, 31, v72
	s_waitcnt lgkmcnt(0)
	v_lshl_add_u64 v[70:71], s[4:5], 0, v[2:3]
	v_lshlrev_b64 v[2:3], 11, v[72:73]
	v_lshl_add_u64 v[2:3], v[70:71], 0, v[2:3]
	v_lshlrev_b32_e32 v74, 8, v82
	global_load_dwordx4 v[84:87], v[2:3], off
	global_load_dwordx4 v[62:65], v74, s[6:7]
	global_load_dwordx4 v[58:61], v74, s[6:7] offset:16
	global_load_dwordx4 v[54:57], v74, s[6:7] offset:32
	global_load_dwordx4 v[50:53], v74, s[6:7] offset:48
	global_load_dwordx4 v[66:69], v[2:3], off offset:16
	s_mov_b64 s[90:91], 0x1000
	v_lshl_add_u64 v[104:105], v[2:3], 0, s[90:91]
	global_load_dword v106, v[104:105], off offset:-2048
	global_load_dword v106, v[104:105], off
	global_load_dword v106, v[104:105], off offset:2048
	v_lshl_add_u64 v[104:105], v[104:105], 0, s[90:91]
	global_load_dword v106, v[104:105], off
	global_load_dword v106, v[104:105], off offset:2048
	v_lshl_add_u64 v[104:105], v[104:105], 0, s[90:91]
	global_load_dword v106, v[104:105], off
	global_load_dword v106, v[104:105], off offset:2048
	global_load_dwordx4 v[46:49], v74, s[6:7] offset:64
	global_load_dwordx4 v[42:45], v74, s[6:7] offset:80
	global_load_dwordx4 v[26:29], v74, s[6:7] offset:112
	global_load_dwordx4 v[38:41], v74, s[6:7] offset:96
	v_lshrrev_b32_e32 v1, 1, v0
	v_mbcnt_lo_u32_b32 v2, -1, 0
	v_and_b32_e32 v91, 28, v1
	v_mbcnt_hi_u32_b32 v1, -1, v2
	v_and_b32_e32 v2, 64, v1
	v_xor_b32_e32 v3, 32, v1
	v_add_u32_e32 v2, 64, v2
	v_xor_b32_e32 v4, 16, v1
	v_cmp_lt_i32_e32 vcc, v3, v2
	v_xor_b32_e32 v5, 8, v1
	v_xor_b32_e32 v6, 4, v1
	v_cndmask_b32_e32 v75, v1, v3, vcc
	v_cmp_lt_i32_e32 vcc, v4, v2
	global_load_dwordx4 v[18:21], v74, s[6:7] offset:144
	global_load_dwordx4 v[30:33], v74, s[6:7] offset:128
	v_cndmask_b32_e32 v76, v1, v4, vcc
	v_cmp_lt_i32_e32 vcc, v5, v2
	v_xor_b32_e32 v7, 2, v1
	v_xor_b32_e32 v8, 1, v1
	v_cndmask_b32_e32 v77, v1, v5, vcc
	v_cmp_lt_i32_e32 vcc, v6, v2
	v_lshlrev_b32_e32 v78, 2, v76
	v_lshlrev_b32_e32 v79, 2, v75
	v_cndmask_b32_e32 v83, v1, v6, vcc
	v_cmp_lt_i32_e32 vcc, v7, v2
	v_lshlrev_b32_e32 v76, 2, v83
	v_lshlrev_b32_e32 v77, 2, v77
	v_cndmask_b32_e32 v92, v1, v7, vcc
	v_cmp_lt_i32_e32 vcc, v8, v2
	v_lshlrev_b32_e32 v75, 2, v92
	v_and_b32_e32 v88, 32, v0
	v_cndmask_b32_e32 v93, v1, v8, vcc
	global_load_dwordx4 v[22:25], v74, s[6:7] offset:176
	global_load_dwordx4 v[34:37], v74, s[6:7] offset:160
	global_load_dwordx4 v[2:5], v74, s[6:7] offset:240
	global_load_dwordx4 v[6:9], v74, s[6:7] offset:224
	global_load_dwordx4 v[10:13], v74, s[6:7] offset:208
	global_load_dwordx4 v[14:17], v74, s[6:7] offset:192
	global_load_dword v73, v91, s[8:9]
	v_lshlrev_b32_e32 v74, 2, v93
	v_cmp_eq_u32_e64 s[8:9], 0, v88
	v_and_b32_e32 v89, 16, v0
	v_cmp_eq_u32_e64 s[2:3], 0, v89
	v_and_b32_e32 v90, 8, v0
	v_cmp_eq_u32_e64 s[4:5], 0, v90
	s_load_dwordx2 s[14:15], s[0:1], 0x28
	s_waitcnt vmcnt(18)
	v_add_f32_e32 v83, 0, v84
	v_add_f32_e32 v83, v83, v85
	v_add_f32_e32 v83, v83, v86
	v_add_f32_e32 v83, v83, v87
	s_waitcnt vmcnt(17)
	v_fma_f32 v92, v62, v84, 0
	s_waitcnt vmcnt(13)
	v_add_f32_e32 v83, v83, v66
	v_add_f32_e32 v83, v83, v67
	v_add_f32_e32 v83, v83, v68
	v_add_f32_e32 v83, v83, v69
	ds_bpermute_b32 v100, v79, v83
	v_fma_f32 v93, v63, v84, 0
	v_fma_f32 v94, v64, v84, 0
	v_fma_f32 v95, v65, v84, 0
	v_fma_f32 v96, v58, v84, 0
	s_waitcnt lgkmcnt(0)
	v_add_f32_e32 v83, v83, v100
	ds_bpermute_b32 v100, v78, v83
	v_fma_f32 v97, v59, v84, 0
	v_fma_f32 v98, v60, v84, 0
	v_fma_f32 v99, v61, v84, 0
	v_fmac_f32_e32 v92, v54, v85
	s_waitcnt lgkmcnt(0)
	v_add_f32_e32 v83, v83, v100
	ds_bpermute_b32 v100, v77, v83
	v_fmac_f32_e32 v93, v55, v85
	v_fmac_f32_e32 v94, v56, v85
	v_fmac_f32_e32 v95, v57, v85
	v_fmac_f32_e32 v96, v50, v85
	s_waitcnt lgkmcnt(0)
	v_add_f32_e32 v83, v83, v100
	ds_bpermute_b32 v100, v76, v83
	v_fmac_f32_e32 v97, v51, v85
	v_fmac_f32_e32 v98, v52, v85
	v_fmac_f32_e32 v99, v53, v85
	s_waitcnt vmcnt(12)
	v_fmac_f32_e32 v92, v46, v86
	s_waitcnt lgkmcnt(0)
	v_add_f32_e32 v83, v83, v100
	ds_bpermute_b32 v100, v75, v83
	v_fmac_f32_e32 v93, v47, v86
	v_fmac_f32_e32 v94, v48, v86
	v_fmac_f32_e32 v95, v49, v86
	s_waitcnt vmcnt(11)
	v_fmac_f32_e32 v96, v42, v86
	s_waitcnt lgkmcnt(0)
	v_add_f32_e32 v83, v83, v100
	ds_bpermute_b32 v100, v74, v83
	v_fmac_f32_e32 v97, v43, v86
	v_fmac_f32_e32 v98, v44, v86
	v_fmac_f32_e32 v99, v45, v86
	s_waitcnt vmcnt(9)
	v_fmac_f32_e32 v92, v38, v87
	s_waitcnt lgkmcnt(0)
	v_add_f32_e32 v83, v83, v100
	v_fmamk_f32 v85, v83, 0xbb000000, v85
	v_fmamk_f32 v84, v83, 0xbb000000, v84
	v_mul_f32_e32 v85, v85, v85
	v_fmamk_f32 v86, v83, 0xbb000000, v86
	v_fmac_f32_e32 v85, v84, v84
	v_fmac_f32_e32 v93, v39, v87
	v_fmac_f32_e32 v94, v40, v87
	v_fmac_f32_e32 v95, v41, v87
	v_fmac_f32_e32 v96, v26, v87
	v_fmac_f32_e32 v97, v27, v87
	v_fmac_f32_e32 v98, v28, v87
	v_fmac_f32_e32 v99, v29, v87
	v_fmamk_f32 v87, v83, 0xbb000000, v87
	v_fmac_f32_e32 v85, v86, v86
	v_fmamk_f32 v100, v83, 0xbb000000, v66
	v_fmac_f32_e32 v85, v87, v87
	v_fmamk_f32 v101, v83, 0xbb000000, v67
	v_fmac_f32_e32 v85, v100, v100
	v_fmamk_f32 v102, v83, 0xbb000000, v68
	v_fmac_f32_e32 v85, v101, v101
	v_fmamk_f32 v103, v83, 0xbb000000, v69
	v_fmac_f32_e32 v85, v102, v102
	s_waitcnt vmcnt(7)
	v_fmac_f32_e32 v92, v30, v66
	v_fmac_f32_e32 v96, v18, v66
	v_fmac_f32_e32 v85, v103, v103
	v_fmac_f32_e32 v93, v31, v66
	v_fmac_f32_e32 v97, v19, v66
	ds_bpermute_b32 v84, v79, v85
	s_waitcnt vmcnt(5)
	v_fmac_f32_e32 v92, v34, v67
	v_fmac_f32_e32 v96, v22, v67
	v_fmac_f32_e32 v94, v32, v66
	v_fmac_f32_e32 v95, v33, v66
	v_fmac_f32_e32 v98, v20, v66
	v_fmac_f32_e32 v99, v21, v66
	v_fmac_f32_e32 v93, v35, v67
	v_fmac_f32_e32 v97, v23, v67
	s_waitcnt vmcnt(1)
	v_fmac_f32_e32 v92, v14, v68
	v_fmac_f32_e32 v96, v10, v68
	v_fmac_f32_e32 v94, v36, v67
	v_fmac_f32_e32 v95, v37, v67
	v_fmac_f32_e32 v98, v24, v67
	v_fmac_f32_e32 v99, v25, v67
	v_fmac_f32_e32 v93, v15, v68
	v_fmac_f32_e32 v97, v11, v68
	v_fmac_f32_e32 v92, v6, v69
	v_fmac_f32_e32 v96, v2, v69
	v_fmac_f32_e32 v94, v16, v68
	v_fmac_f32_e32 v95, v17, v68
	v_fmac_f32_e32 v98, v12, v68
	v_fmac_f32_e32 v99, v13, v68
	v_fmac_f32_e32 v93, v7, v69
	v_cndmask_b32_e64 v68, v92, v96, s[8:9]
	v_fmac_f32_e32 v97, v3, v69
	v_fmac_f32_e32 v94, v8, v69
	ds_bpermute_b32 v68, v79, v68
	v_fmac_f32_e32 v95, v9, v69
	v_fmac_f32_e32 v98, v4, v69
	v_fmac_f32_e32 v99, v5, v69
	v_cndmask_b32_e64 v69, v93, v97, s[8:9]
	s_waitcnt lgkmcnt(1)
	v_add_f32_e32 v66, v85, v84
	ds_bpermute_b32 v69, v79, v69
	v_cndmask_b32_e64 v85, v94, v98, s[8:9]
	ds_bpermute_b32 v85, v79, v85
	v_cndmask_b32_e64 v86, v95, v99, s[8:9]
	ds_bpermute_b32 v86, v79, v86
	v_cndmask_b32_e64 v67, v96, v92, s[8:9]
	s_waitcnt lgkmcnt(3)
	v_add_f32_e32 v67, v67, v68
	v_cndmask_b32_e64 v68, v97, v93, s[8:9]
	s_waitcnt lgkmcnt(2)
	v_add_f32_e32 v68, v68, v69
	v_cndmask_b32_e64 v69, v98, v94, s[8:9]
	s_waitcnt lgkmcnt(1)
	v_add_f32_e32 v69, v69, v85
	v_cndmask_b32_e64 v85, v99, v95, s[8:9]
	s_waitcnt lgkmcnt(0)
	v_add_f32_e32 v85, v85, v86
	v_cndmask_b32_e64 v86, v69, v67, s[2:3]
	v_cndmask_b32_e64 v67, v67, v69, s[2:3]
	v_cndmask_b32_e64 v69, v68, v85, s[2:3]
	ds_bpermute_b32 v67, v78, v67
	ds_bpermute_b32 v69, v78, v69
	ds_bpermute_b32 v84, v78, v66
	v_cndmask_b32_e64 v68, v85, v68, s[2:3]
	s_waitcnt lgkmcnt(2)
	v_add_f32_e32 v67, v86, v67
	s_waitcnt lgkmcnt(1)
	v_add_f32_e32 v68, v68, v69
	s_waitcnt lgkmcnt(0)
	v_add_f32_e32 v66, v66, v84
	v_cndmask_b32_e64 v69, v68, v67, s[4:5]
	v_cndmask_b32_e64 v67, v67, v68, s[4:5]
	ds_bpermute_b32 v84, v77, v66
	ds_bpermute_b32 v67, v77, v67
	s_waitcnt lgkmcnt(1)
	v_add_f32_e32 v66, v66, v84
	s_waitcnt lgkmcnt(0)
	v_add_f32_e32 v67, v69, v67
	ds_bpermute_b32 v68, v76, v66
	ds_bpermute_b32 v69, v76, v67
	s_waitcnt lgkmcnt(1)
	v_add_f32_e32 v66, v66, v68
	s_waitcnt lgkmcnt(0)
	v_add_f32_e32 v69, v67, v69
	ds_bpermute_b32 v68, v75, v66
	ds_bpermute_b32 v84, v75, v69
	s_waitcnt lgkmcnt(1)
	v_add_f32_e32 v66, v66, v68
	s_waitcnt lgkmcnt(0)
	v_add_f32_e32 v84, v69, v84
	ds_bpermute_b32 v67, v74, v66
	ds_bpermute_b32 v85, v74, v84
	v_and_b32_e32 v68, 7, v0
	v_cmp_eq_u32_e64 s[6:7], 0, v68
	v_or_b32_e32 v68, 0x8200, v91
	v_mad_u32_u24 v69, v81, 36, v68
	s_and_saveexec_b64 s[10:11], s[6:7]
	s_cbranch_execz .LBB7_9
	s_waitcnt lgkmcnt(0)
	v_add_f32_e32 v84, v84, v85
	s_waitcnt vmcnt(0)
	v_add_f32_e32 v84, v73, v84
	ds_write_b32 v69, v84

	.amdhsa_kernel _Z18fused_router_wprepILb1EEvPKfS1_S1_PKiPfS4_PiS5_S5_S5_S4_S1_PDF16_S6_S1_S6_
		.amdhsa_group_segment_fixed_size 34432
		.amdhsa_private_segment_fixed_size 0
		.amdhsa_kernarg_size 128
		.amdhsa_user_sgpr_count 2
		.amdhsa_user_sgpr_dispatch_ptr 0
		.amdhsa_user_sgpr_queue_ptr 0
		.amdhsa_user_sgpr_kernarg_segment_ptr 1
		.amdhsa_user_sgpr_dispatch_id 0
		.amdhsa_user_sgpr_kernarg_preload_length 0
		.amdhsa_user_sgpr_kernarg_preload_offset 0
		.amdhsa_user_sgpr_private_segment_size 0
		.amdhsa_uses_dynamic_stack 0
		.amdhsa_enable_private_segment 0
		.amdhsa_system_sgpr_workgroup_id_x 1
		.amdhsa_system_sgpr_workgroup_id_y 0
		.amdhsa_system_sgpr_workgroup_id_z 0
		.amdhsa_system_sgpr_workgroup_info 0
		.amdhsa_system_vgpr_workitem_id 0
		.amdhsa_next_free_vgpr 107
		.amdhsa_next_free_sgpr 96
		.amdhsa_accum_offset 108
		.amdhsa_reserve_vcc 1
		.amdhsa_float_round_mode_32 0
		.amdhsa_float_round_mode_16_64 0
		.amdhsa_float_denorm_mode_32 3
		.amdhsa_float_denorm_mode_16_64 3
		.amdhsa_dx10_clamp 1
		.amdhsa_ieee_mode 1
		.amdhsa_fp16_overflow 0
		.amdhsa_tg_split 0
		.amdhsa_exception_fp_ieee_invalid_op 0
		.amdhsa_exception_fp_denorm_src 0
		.amdhsa_exception_fp_ieee_div_zero 0
		.amdhsa_exception_fp_ieee_overflow 0
		.amdhsa_exception_fp_ieee_underflow 0
		.amdhsa_exception_fp_ieee_inexact 0
		.amdhsa_exception_int_div_zero 0
	.end_amdhsa_kernel

.LBB8_6:
	s_andn2_b64 vcc, exec, s[4:5]
	s_cbranch_vccnz .LBB8_70
	s_load_dwordx4 s[4:7], s[0:1], 0x0
	s_load_dwordx2 s[8:9], s[0:1], 0x10
	v_lshrrev_b32_e32 v78, 3, v0
	v_and_b32_e32 v87, 24, v78
	s_lshl_b32 s24, s2, 5
	v_and_b32_e32 v89, 63, v0
	v_or_b32_e32 v76, s24, v87
	v_lshlrev_b32_e32 v2, 5, v89
	v_mov_b32_e32 v3, 0
	v_ashrrev_i32_e32 v77, 31, v76
	s_waitcnt lgkmcnt(0)
	v_lshl_add_u64 v[74:75], s[4:5], 0, v[2:3]
	v_lshlrev_b64 v[2:3], 11, v[76:77]
	v_lshl_add_u64 v[34:35], v[74:75], 0, v[2:3]
	global_load_dwordx4 v[70:73], v[34:35], off
	v_lshlrev_b32_e32 v77, 8, v89
	global_load_dwordx4 v[22:25], v77, s[6:7]
	global_load_dwordx4 v[18:21], v77, s[6:7] offset:16
	global_load_dwordx4 v[14:17], v77, s[6:7] offset:32
	global_load_dwordx4 v[10:13], v77, s[6:7] offset:48
	global_load_dwordx4 v[6:9], v77, s[6:7] offset:64
	global_load_dwordx4 v[2:5], v77, s[6:7] offset:80
	global_load_dwordx4 v[66:69], v[34:35], off offset:16
	s_mov_b64 s[90:91], 0x1000
	v_lshl_add_u64 v[100:101], v[34:35], 0, s[90:91]
	global_load_dword v102, v[100:101], off offset:-2048
	global_load_dword v102, v[100:101], off
	global_load_dword v102, v[100:101], off offset:2048
	v_lshl_add_u64 v[100:101], v[100:101], 0, s[90:91]
	global_load_dword v102, v[100:101], off
	global_load_dword v102, v[100:101], off offset:2048
	v_lshl_add_u64 v[100:101], v[100:101], 0, s[90:91]
	global_load_dword v102, v[100:101], off
	global_load_dword v102, v[100:101], off offset:2048
	global_load_dwordx4 v[26:29], v77, s[6:7] offset:96
	global_load_dwordx4 v[30:33], v77, s[6:7] offset:112
	v_mbcnt_lo_u32_b32 v1, -1, 0
	v_mbcnt_hi_u32_b32 v1, -1, v1
	v_and_b32_e32 v42, 64, v1
	v_xor_b32_e32 v46, 32, v1
	v_add_u32_e32 v53, 64, v42
	v_xor_b32_e32 v47, 16, v1
	v_cmp_lt_i32_e32 vcc, v46, v53
	v_xor_b32_e32 v48, 8, v1
	v_xor_b32_e32 v50, 4, v1
	v_cndmask_b32_e32 v54, v1, v46, vcc
	v_cmp_lt_i32_e32 vcc, v47, v53
	v_xor_b32_e32 v51, 2, v1
	global_load_dwordx4 v[34:37], v77, s[6:7] offset:128
	global_load_dwordx4 v[38:41], v77, s[6:7] offset:144
	v_cndmask_b32_e32 v55, v1, v47, vcc
	v_cmp_lt_i32_e32 vcc, v48, v53
	v_xor_b32_e32 v52, 1, v1
	global_load_dwordx4 v[42:45], v77, s[6:7] offset:160
	v_cndmask_b32_e32 v56, v1, v48, vcc
	v_cmp_lt_i32_e32 vcc, v50, v53
	global_load_dwordx4 v[46:49], v77, s[6:7] offset:176
	global_load_dwordx4 v[62:65], v77, s[6:7] offset:208
	v_cndmask_b32_e32 v57, v1, v50, vcc
	v_cmp_lt_i32_e32 vcc, v51, v53
	v_lshlrev_b32_e32 v84, 2, v54
	v_lshlrev_b32_e32 v81, 2, v55
	v_cndmask_b32_e32 v58, v1, v51, vcc
	v_cmp_lt_i32_e32 vcc, v52, v53
	v_lshlrev_b32_e32 v83, 2, v56
	v_lshlrev_b32_e32 v80, 2, v57
	v_cndmask_b32_e32 v59, v1, v52, vcc
	global_load_dwordx4 v[50:53], v77, s[6:7] offset:192
	v_lshlrev_b32_e32 v79, 2, v58
	v_lshlrev_b32_e32 v82, 2, v59
	global_load_dwordx4 v[58:61], v77, s[6:7] offset:224
	global_load_dwordx4 v[54:57], v77, s[6:7] offset:240
	s_load_dwordx2 s[14:15], s[0:1], 0x28
	s_waitcnt vmcnt(17)
	v_add_f32_e32 v77, 0, v70
	v_add_f32_e32 v77, v77, v71
	v_add_f32_e32 v77, v77, v72
	v_add_f32_e32 v77, v77, v73
	s_waitcnt vmcnt(10)
	v_add_f32_e32 v77, v77, v66
	v_add_f32_e32 v77, v77, v67
	v_add_f32_e32 v77, v77, v68
	v_add_f32_e32 v77, v77, v69
	ds_bpermute_b32 v85, v84, v77
	v_fma_f32 v86, v22, v70, 0
	v_fma_f32 v88, v23, v70, 0
	v_fma_f32 v90, v24, v70, 0
	v_fma_f32 v91, v25, v70, 0
	s_waitcnt lgkmcnt(0)
	v_add_f32_e32 v77, v77, v85
	ds_bpermute_b32 v85, v81, v77
	v_fma_f32 v92, v18, v70, 0
	v_fma_f32 v93, v19, v70, 0
	v_fma_f32 v94, v20, v70, 0
	v_fma_f32 v95, v21, v70, 0
	s_waitcnt lgkmcnt(0)
	v_add_f32_e32 v77, v77, v85
	ds_bpermute_b32 v85, v83, v77
	v_fmac_f32_e32 v86, v14, v71
	v_fmac_f32_e32 v88, v15, v71
	v_fmac_f32_e32 v90, v16, v71
	v_fmac_f32_e32 v91, v17, v71
	s_waitcnt lgkmcnt(0)
	v_add_f32_e32 v77, v77, v85
	ds_bpermute_b32 v85, v80, v77
	v_fmac_f32_e32 v92, v10, v71
	v_fmac_f32_e32 v93, v11, v71
	v_fmac_f32_e32 v94, v12, v71
	v_fmac_f32_e32 v95, v13, v71
	s_waitcnt lgkmcnt(0)
	v_add_f32_e32 v77, v77, v85
	ds_bpermute_b32 v85, v79, v77
	v_fmac_f32_e32 v86, v6, v72
	v_fmac_f32_e32 v88, v7, v72
	v_fmac_f32_e32 v90, v8, v72
	v_fmac_f32_e32 v91, v9, v72
	s_waitcnt lgkmcnt(0)
	v_add_f32_e32 v77, v77, v85
	ds_bpermute_b32 v85, v82, v77
	v_fmac_f32_e32 v92, v2, v72
	v_fmac_f32_e32 v93, v3, v72
	v_fmac_f32_e32 v94, v4, v72
	v_fmac_f32_e32 v95, v5, v72
	s_waitcnt lgkmcnt(0)
	v_add_f32_e32 v77, v77, v85
	v_lshrrev_b32_e32 v85, 1, v0
	v_and_b32_e32 v96, 28, v85
	global_load_dword v85, v96, s[8:9]
	v_fmamk_f32 v71, v77, 0xbb000000, v71
	v_fmamk_f32 v70, v77, 0xbb000000, v70
	v_mul_f32_e32 v71, v71, v71
	v_fmamk_f32 v72, v77, 0xbb000000, v72
	v_fmac_f32_e32 v71, v70, v70
	s_waitcnt vmcnt(10)
	v_fmac_f32_e32 v86, v26, v73
	v_fmac_f32_e32 v88, v27, v73
	v_fmac_f32_e32 v90, v28, v73
	v_fmac_f32_e32 v91, v29, v73
	s_waitcnt vmcnt(9)
	v_fmac_f32_e32 v92, v30, v73
	v_fmac_f32_e32 v93, v31, v73
	v_fmac_f32_e32 v94, v32, v73
	v_fmac_f32_e32 v95, v33, v73
	v_fmamk_f32 v73, v77, 0xbb000000, v73
	v_fmac_f32_e32 v71, v72, v72
	s_waitcnt vmcnt(8)
	v_fmac_f32_e32 v86, v34, v66
	v_fmac_f32_e32 v88, v35, v66
	v_fmac_f32_e32 v90, v36, v66
	v_fmac_f32_e32 v91, v37, v66
	s_waitcnt vmcnt(7)
	v_fmac_f32_e32 v92, v38, v66
	v_fmac_f32_e32 v93, v39, v66
	v_fmac_f32_e32 v94, v40, v66
	v_fmac_f32_e32 v95, v41, v66
	v_fmamk_f32 v66, v77, 0xbb000000, v66
	v_fmac_f32_e32 v71, v73, v73
	s_waitcnt vmcnt(6)
	v_fmac_f32_e32 v86, v42, v67
	v_fmac_f32_e32 v88, v43, v67
	v_fmac_f32_e32 v90, v44, v67
	v_fmac_f32_e32 v91, v45, v67
	s_waitcnt vmcnt(5)
	v_fmac_f32_e32 v92, v46, v67
	v_fmac_f32_e32 v93, v47, v67
	v_fmac_f32_e32 v94, v48, v67
	v_fmac_f32_e32 v95, v49, v67
	v_fmamk_f32 v67, v77, 0xbb000000, v67
	v_fmac_f32_e32 v71, v66, v66
	s_waitcnt vmcnt(3)
	v_fmac_f32_e32 v86, v50, v68
	v_fmac_f32_e32 v88, v51, v68
	v_fmac_f32_e32 v90, v52, v68
	v_fmac_f32_e32 v91, v53, v68
	v_fmac_f32_e32 v92, v62, v68
	v_fmac_f32_e32 v93, v63, v68
	v_fmac_f32_e32 v94, v64, v68
	v_fmac_f32_e32 v95, v65, v68
	v_fmamk_f32 v68, v77, 0xbb000000, v68
	v_fmac_f32_e32 v71, v67, v67
	v_fmamk_f32 v97, v77, 0xbb000000, v69
	v_fmac_f32_e32 v71, v68, v68
	v_fmac_f32_e32 v71, v97, v97
	ds_bpermute_b32 v66, v84, v71
	v_and_b32_e32 v67, 32, v0
	s_waitcnt vmcnt(2)
	v_fmac_f32_e32 v86, v58, v69
	s_waitcnt vmcnt(1)
	v_fmac_f32_e32 v92, v54, v69
	v_cmp_eq_u32_e64 s[10:11], 0, v67
	v_fmac_f32_e32 v88, v59, v69
	v_fmac_f32_e32 v93, v55, v69
	v_cndmask_b32_e64 v68, v86, v92, s[10:11]
	v_fmac_f32_e32 v90, v60, v69
	ds_bpermute_b32 v68, v84, v68
	v_fmac_f32_e32 v94, v56, v69
	v_cndmask_b32_e64 v70, v88, v93, s[10:11]
	v_fmac_f32_e32 v91, v61, v69
	v_fmac_f32_e32 v95, v57, v69
	s_waitcnt lgkmcnt(1)
	v_add_f32_e32 v66, v71, v66
	ds_bpermute_b32 v70, v84, v70
	v_cndmask_b32_e64 v71, v90, v94, s[10:11]
	ds_bpermute_b32 v71, v84, v71
	v_cndmask_b32_e64 v72, v91, v95, s[10:11]
	ds_bpermute_b32 v72, v84, v72
	v_cndmask_b32_e64 v67, v92, v86, s[10:11]
	s_waitcnt lgkmcnt(3)
	v_add_f32_e32 v67, v67, v68
	v_cndmask_b32_e64 v68, v93, v88, s[10:11]
	s_waitcnt lgkmcnt(2)
	v_add_f32_e32 v68, v68, v70
	v_cndmask_b32_e64 v70, v94, v90, s[10:11]
	s_waitcnt lgkmcnt(1)
	v_add_f32_e32 v70, v70, v71
	v_cndmask_b32_e64 v71, v95, v91, s[10:11]
	s_waitcnt lgkmcnt(0)
	v_add_f32_e32 v71, v71, v72
	v_and_b32_e32 v72, 16, v0
	v_cmp_eq_u32_e64 s[2:3], 0, v72
	ds_bpermute_b32 v69, v81, v66
	v_or_b32_e32 v86, 0x4100, v96
	v_cndmask_b32_e64 v72, v70, v67, s[2:3]
	v_cndmask_b32_e64 v67, v67, v70, s[2:3]
	v_cndmask_b32_e64 v70, v68, v71, s[2:3]
	ds_bpermute_b32 v70, v81, v70
	ds_bpermute_b32 v67, v81, v67
	v_cndmask_b32_e64 v68, v71, v68, s[2:3]
	s_waitcnt lgkmcnt(2)
	v_add_f32_e32 v66, v66, v69
	ds_bpermute_b32 v69, v83, v66
	s_waitcnt lgkmcnt(2)
	v_add_f32_e32 v68, v68, v70
	v_and_b32_e32 v70, 8, v0
	s_waitcnt lgkmcnt(1)
	v_add_f32_e32 v67, v72, v67
	v_cmp_eq_u32_e64 s[4:5], 0, v70
	s_waitcnt lgkmcnt(0)
	v_add_f32_e32 v66, v66, v69
	v_mad_u32_u24 v88, v87, 36, v86
	v_cndmask_b32_e64 v70, v68, v67, s[4:5]
	v_cndmask_b32_e64 v67, v67, v68, s[4:5]
	ds_bpermute_b32 v67, v83, v67
	ds_bpermute_b32 v68, v80, v66
	s_waitcnt lgkmcnt(1)
	v_add_f32_e32 v67, v70, v67
	ds_bpermute_b32 v69, v80, v67
	s_waitcnt lgkmcnt(1)
	v_add_f32_e32 v66, v66, v68
	ds_bpermute_b32 v68, v79, v66
	v_and_b32_e32 v70, 7, v0
	v_cmp_eq_u32_e64 s[6:7], 0, v70
	s_waitcnt lgkmcnt(1)
	v_add_f32_e32 v67, v67, v69
	ds_bpermute_b32 v69, v79, v67
	s_waitcnt lgkmcnt(1)
	v_add_f32_e32 v66, v66, v68
	s_waitcnt lgkmcnt(0)
	v_add_f32_e32 v68, v67, v69
	ds_bpermute_b32 v67, v82, v66
	ds_bpermute_b32 v69, v82, v68
	s_and_saveexec_b64 s[8:9], s[6:7]
	s_cbranch_execz .LBB8_9
	s_waitcnt lgkmcnt(0)
	v_add_f32_e32 v68, v68, v69
	s_waitcnt vmcnt(0)
	v_add_f32_e32 v68, v85, v68
	ds_write_b32 v88, v68

	.amdhsa_kernel _Z18fused_router_wprepILb0EEvPKfS1_S1_PKiPfS4_PiS5_S5_S5_S4_S1_PDF16_S6_S1_S6_
		.amdhsa_group_segment_fixed_size 17792
		.amdhsa_private_segment_fixed_size 0
		.amdhsa_kernarg_size 128
		.amdhsa_user_sgpr_count 2
		.amdhsa_user_sgpr_dispatch_ptr 0
		.amdhsa_user_sgpr_queue_ptr 0
		.amdhsa_user_sgpr_kernarg_segment_ptr 1
		.amdhsa_user_sgpr_dispatch_id 0
		.amdhsa_user_sgpr_kernarg_preload_length 0
		.amdhsa_user_sgpr_kernarg_preload_offset 0
		.amdhsa_user_sgpr_private_segment_size 0
		.amdhsa_uses_dynamic_stack 0
		.amdhsa_enable_private_segment 0
		.amdhsa_system_sgpr_workgroup_id_x 1
		.amdhsa_system_sgpr_workgroup_id_y 0
		.amdhsa_system_sgpr_workgroup_id_z 0
		.amdhsa_system_sgpr_workgroup_info 0
		.amdhsa_system_vgpr_workitem_id 0
		.amdhsa_next_free_vgpr 103
		.amdhsa_next_free_sgpr 96
		.amdhsa_accum_offset 104
		.amdhsa_reserve_vcc 1
		.amdhsa_float_round_mode_32 0
		.amdhsa_float_round_mode_16_64 0
		.amdhsa_float_denorm_mode_32 3
		.amdhsa_float_denorm_mode_16_64 3
		.amdhsa_dx10_clamp 1
		.amdhsa_ieee_mode 1
		.amdhsa_fp16_overflow 0
		.amdhsa_tg_split 0
		.amdhsa_exception_fp_ieee_invalid_op 0
		.amdhsa_exception_fp_denorm_src 0
		.amdhsa_exception_fp_ieee_div_zero 0
		.amdhsa_exception_fp_ieee_overflow 0
		.amdhsa_exception_fp_ieee_underflow 0
		.amdhsa_exception_fp_ieee_inexact 0
		.amdhsa_exception_int_div_zero 0
	.end_amdhsa_kernel
